# speedup vs baseline: 1.0653x; 1.0279x over previous
.LBB0_2:
	s_or_b64 exec, exec, s[10:11]
	s_load_dwordx2 s[8:9], s[0:1], 0x10
	v_and_b32_e32 v34, 63, v0
	v_lshrrev_b32_e32 v39, 6, v0
	v_mov_b32_e32 v38, 0x3c0
	v_cmp_eq_u32_e64 s[6:7], 0, v34
	v_mad_u32_u24 v38, v39, 48, v38
	v_add_f32_dpp v145, v145, v145 row_ror:8 row_mask:0xf bank_mask:0xf bound_ctrl:1
	v_add_f32_dpp v143, v143, v143 row_ror:8 row_mask:0xf bank_mask:0xf bound_ctrl:1
	v_add_f32_dpp v144, v144, v144 row_ror:8 row_mask:0xf bank_mask:0xf bound_ctrl:1
	v_add_f32_dpp v142, v142, v142 row_ror:8 row_mask:0xf bank_mask:0xf bound_ctrl:1
	v_add_f32_dpp v141, v141, v141 row_ror:8 row_mask:0xf bank_mask:0xf bound_ctrl:1
	v_add_f32_dpp v139, v139, v139 row_ror:8 row_mask:0xf bank_mask:0xf bound_ctrl:1
	v_add_f32_dpp v140, v140, v140 row_ror:8 row_mask:0xf bank_mask:0xf bound_ctrl:1
	v_add_f32_dpp v138, v138, v138 row_ror:8 row_mask:0xf bank_mask:0xf bound_ctrl:1
	v_add_f32_dpp v137, v137, v137 row_ror:8 row_mask:0xf bank_mask:0xf bound_ctrl:1
	v_add_f32_dpp v72, v72, v72 row_ror:8 row_mask:0xf bank_mask:0xf bound_ctrl:1
	v_add_f32_dpp v73, v73, v73 row_ror:8 row_mask:0xf bank_mask:0xf bound_ctrl:1
	v_add_f32_dpp v71, v71, v71 row_ror:8 row_mask:0xf bank_mask:0xf bound_ctrl:1
	v_add_f32_dpp v145, v145, v145 row_ror:4 row_mask:0xf bank_mask:0xf bound_ctrl:1
	v_add_f32_dpp v143, v143, v143 row_ror:4 row_mask:0xf bank_mask:0xf bound_ctrl:1
	v_add_f32_dpp v144, v144, v144 row_ror:4 row_mask:0xf bank_mask:0xf bound_ctrl:1
	v_add_f32_dpp v142, v142, v142 row_ror:4 row_mask:0xf bank_mask:0xf bound_ctrl:1
	v_add_f32_dpp v141, v141, v141 row_ror:4 row_mask:0xf bank_mask:0xf bound_ctrl:1
	v_add_f32_dpp v139, v139, v139 row_ror:4 row_mask:0xf bank_mask:0xf bound_ctrl:1
	v_add_f32_dpp v140, v140, v140 row_ror:4 row_mask:0xf bank_mask:0xf bound_ctrl:1
	v_add_f32_dpp v138, v138, v138 row_ror:4 row_mask:0xf bank_mask:0xf bound_ctrl:1
	v_add_f32_dpp v137, v137, v137 row_ror:4 row_mask:0xf bank_mask:0xf bound_ctrl:1
	v_add_f32_dpp v72, v72, v72 row_ror:4 row_mask:0xf bank_mask:0xf bound_ctrl:1
	v_add_f32_dpp v73, v73, v73 row_ror:4 row_mask:0xf bank_mask:0xf bound_ctrl:1
	v_add_f32_dpp v71, v71, v71 row_ror:4 row_mask:0xf bank_mask:0xf bound_ctrl:1
	v_add_f32_dpp v145, v145, v145 row_ror:2 row_mask:0xf bank_mask:0xf bound_ctrl:1
	v_add_f32_dpp v143, v143, v143 row_ror:2 row_mask:0xf bank_mask:0xf bound_ctrl:1
	v_add_f32_dpp v144, v144, v144 row_ror:2 row_mask:0xf bank_mask:0xf bound_ctrl:1
	v_add_f32_dpp v142, v142, v142 row_ror:2 row_mask:0xf bank_mask:0xf bound_ctrl:1
	v_add_f32_dpp v141, v141, v141 row_ror:2 row_mask:0xf bank_mask:0xf bound_ctrl:1
	v_add_f32_dpp v139, v139, v139 row_ror:2 row_mask:0xf bank_mask:0xf bound_ctrl:1
	v_add_f32_dpp v140, v140, v140 row_ror:2 row_mask:0xf bank_mask:0xf bound_ctrl:1
	v_add_f32_dpp v138, v138, v138 row_ror:2 row_mask:0xf bank_mask:0xf bound_ctrl:1
	v_add_f32_dpp v137, v137, v137 row_ror:2 row_mask:0xf bank_mask:0xf bound_ctrl:1
	v_add_f32_dpp v72, v72, v72 row_ror:2 row_mask:0xf bank_mask:0xf bound_ctrl:1
	v_add_f32_dpp v73, v73, v73 row_ror:2 row_mask:0xf bank_mask:0xf bound_ctrl:1
	v_add_f32_dpp v71, v71, v71 row_ror:2 row_mask:0xf bank_mask:0xf bound_ctrl:1
	v_add_f32_dpp v145, v145, v145 row_ror:1 row_mask:0xf bank_mask:0xf bound_ctrl:1
	v_add_f32_dpp v143, v143, v143 row_ror:1 row_mask:0xf bank_mask:0xf bound_ctrl:1
	v_add_f32_dpp v144, v144, v144 row_ror:1 row_mask:0xf bank_mask:0xf bound_ctrl:1
	v_add_f32_dpp v142, v142, v142 row_ror:1 row_mask:0xf bank_mask:0xf bound_ctrl:1
	v_add_f32_dpp v141, v141, v141 row_ror:1 row_mask:0xf bank_mask:0xf bound_ctrl:1
	v_add_f32_dpp v139, v139, v139 row_ror:1 row_mask:0xf bank_mask:0xf bound_ctrl:1
	v_add_f32_dpp v140, v140, v140 row_ror:1 row_mask:0xf bank_mask:0xf bound_ctrl:1
	v_add_f32_dpp v138, v138, v138 row_ror:1 row_mask:0xf bank_mask:0xf bound_ctrl:1
	v_add_f32_dpp v137, v137, v137 row_ror:1 row_mask:0xf bank_mask:0xf bound_ctrl:1
	v_add_f32_dpp v72, v72, v72 row_ror:1 row_mask:0xf bank_mask:0xf bound_ctrl:1
	v_add_f32_dpp v73, v73, v73 row_ror:1 row_mask:0xf bank_mask:0xf bound_ctrl:1
	v_add_f32_dpp v71, v71, v71 row_ror:1 row_mask:0xf bank_mask:0xf bound_ctrl:1
	v_add_f32_dpp v145, v145, v145 row_bcast:15 row_mask:0xa bank_mask:0xf
	v_add_f32_dpp v143, v143, v143 row_bcast:15 row_mask:0xa bank_mask:0xf
	v_add_f32_dpp v144, v144, v144 row_bcast:15 row_mask:0xa bank_mask:0xf
	v_add_f32_dpp v142, v142, v142 row_bcast:15 row_mask:0xa bank_mask:0xf
	v_add_f32_dpp v141, v141, v141 row_bcast:15 row_mask:0xa bank_mask:0xf
	v_add_f32_dpp v139, v139, v139 row_bcast:15 row_mask:0xa bank_mask:0xf
	v_add_f32_dpp v140, v140, v140 row_bcast:15 row_mask:0xa bank_mask:0xf
	v_add_f32_dpp v138, v138, v138 row_bcast:15 row_mask:0xa bank_mask:0xf
	v_add_f32_dpp v137, v137, v137 row_bcast:15 row_mask:0xa bank_mask:0xf
	v_add_f32_dpp v72, v72, v72 row_bcast:15 row_mask:0xa bank_mask:0xf
	v_add_f32_dpp v73, v73, v73 row_bcast:15 row_mask:0xa bank_mask:0xf
	v_add_f32_dpp v71, v71, v71 row_bcast:15 row_mask:0xa bank_mask:0xf
	v_add_f32_dpp v152, v145, v145 row_bcast:31 row_mask:0xc bank_mask:0xf
	v_add_f32_dpp v153, v143, v143 row_bcast:31 row_mask:0xc bank_mask:0xf
	v_add_f32_dpp v154, v144, v144 row_bcast:31 row_mask:0xc bank_mask:0xf
	v_add_f32_dpp v155, v142, v142 row_bcast:31 row_mask:0xc bank_mask:0xf
	v_add_f32_dpp v156, v141, v141 row_bcast:31 row_mask:0xc bank_mask:0xf
	v_add_f32_dpp v157, v139, v139 row_bcast:31 row_mask:0xc bank_mask:0xf
	v_add_f32_dpp v158, v140, v140 row_bcast:31 row_mask:0xc bank_mask:0xf
	v_add_f32_dpp v159, v138, v138 row_bcast:31 row_mask:0xc bank_mask:0xf
	v_add_f32_dpp v34, v137, v137 row_bcast:31 row_mask:0xc bank_mask:0xf
	v_add_f32_dpp v35, v72, v72 row_bcast:31 row_mask:0xc bank_mask:0xf
	v_add_f32_dpp v36, v73, v73 row_bcast:31 row_mask:0xc bank_mask:0xf
	v_add_f32_dpp v37, v71, v71 row_bcast:31 row_mask:0xc bank_mask:0xf
	s_mov_b32 exec_lo, 0
	s_mov_b32 exec_hi, 0x80000000
	ds_write_b128 v38, v[152:155]
	ds_write_b128 v38, v[156:159] offset:16
	ds_write_b128 v38, v[34:37] offset:32
	s_mov_b64 exec, -1
	v_cmp_gt_u32_e32 vcc, 12, v0
	v_lshlrev_b32_e32 v34, 2, v0
	s_waitcnt lgkmcnt(0)
	s_barrier
	s_load_dwordx4 s[12:15], s[0:1], 0x20
	s_load_dwordx2 s[10:11], s[0:1], 0x18
	s_mov_b32 s20, 0
	s_mov_b32 s21, 0xc1f00000
	s_mov_b32 s23, 0xffffffe0
	s_and_saveexec_b64 s[16:17], vcc
	s_cbranch_execz .Lkf_pub_done
	ds_read2_b32 v[36:37], v34 offset0:240 offset1:252
	v_add_u32_e32 v35, 0x400, v34
	ds_read2_b32 v[42:43], v35 offset0:8 offset1:20
	ds_read2_b32 v[44:45], v35 offset0:32 offset1:44
	ds_read2_b32 v[48:49], v35 offset0:56 offset1:68
	ds_read2_b32 v[52:53], v35 offset0:80 offset1:92
	ds_read2_b32 v[152:153], v35 offset0:104 offset1:116
	s_mul_i32 s18, s2, 48
	s_mul_hi_i32 s19, s2, 48
	s_waitcnt lgkmcnt(0)
	v_add_f32_e32 v36, 0, v36
	v_add_f32_e32 v36, v36, v37
	v_add_f32_e32 v36, v36, v42
	v_add_f32_e32 v36, v36, v43
	v_add_f32_e32 v36, v36, v44
	v_add_f32_e32 v36, v36, v45
	v_add_f32_e32 v36, v36, v48
	v_add_f32_e32 v36, v36, v49
	v_add_f32_e32 v36, v36, v52
	v_add_f32_e32 v36, v36, v53
	v_add_f32_e32 v36, v36, v152
	s_add_u32 s18, s8, s18
	v_add_f32_e32 v35, v36, v153
	s_addc_u32 s19, s9, s19
	v_and_b32_e32 v38, 3, v0
	v_lshrrev_b32_e32 v41, 2, v0
	global_store_dword v34, v35, s[18:19] sc1
	v_cmp_ne_u32_e32 vcc, 3, v38
	s_and_b64 exec, exec, vcc
	s_cbranch_execz .Lkf_pub_done
	v_cmp_eq_u32_e32 vcc, 0, v38
	v_cvt_f64_f32_e32 v[42:43], v35
	s_lshl_b32 s18, s24, 4
	s_add_i32 s18, s18, s3
	v_cndmask_b32_e64 v37, 24, 0, vcc
	v_ldexp_f64 v[42:43], v[42:43], v37
	s_mulk_i32 s18, 0x60
	v_lshlrev_b32_e32 v41, 5, v41
	v_ldexp_f64 v[44:45], v[42:43], s23
	v_lshl_add_u32 v41, v38, 3, v41
	v_floor_f64_e32 v[44:45], v[44:45]
	v_add_u32_e32 v41, s18, v41
	v_fma_f64 v[48:49], v[44:45], s[20:21], v[42:43]
	v_cvt_i32_f64_e32 v37, v[44:45]
	v_cvt_u32_f64_e32 v36, v[48:49]
	s_nop 0
	v_lshlrev_b64 v[36:37], 8, v[36:37]
	s_nop 0
	v_or_b32_e32 v36, 1, v36
	s_nop 0
	global_atomic_add_x2 v41, v[36:37], s[14:15]

_Z9k4_reducePKjP15HIP_vector_typeIjLj2EE:
	s_load_dwordx4 s[4:7], s[0:1], 0x0
	s_cmp_ge_u32 s2, 0xc0
	s_cselect_b32 s8, 1, 0
	s_mul_i32 s9, s8, 0xc0
	s_sub_u32 s9, s2, s9
	s_lshl_b32 s9, s9, 8
	s_mul_i32 s10, s8, 0x600000
	s_add_u32 s9, s9, s10
	s_mov_b32 s11, 0x60000
	v_and_b32_e32 v1, 15, v0
	v_lshrrev_b32_e32 v2, 4, v0
	v_lshlrev_b32_e32 v3, 4, v1
	v_mad_u32_u24 v3, v2, s11, v3
	s_waitcnt lgkmcnt(0)
	s_add_u32 s12, s4, s9
	s_addc_u32 s13, s5, 0
	s_add_u32 s14, s12, 0xc000
	s_addc_u32 s15, s13, 0
	s_add_u32 s16, s14, 0xc000
	s_addc_u32 s17, s15, 0
	s_add_u32 s18, s16, 0xc000
	s_addc_u32 s19, s17, 0
	s_add_u32 s20, s18, 0xc000
	s_addc_u32 s21, s19, 0
	s_add_u32 s22, s20, 0xc000
	s_addc_u32 s23, s21, 0
	s_add_u32 s24, s22, 0xc000
	s_addc_u32 s25, s23, 0
	s_add_u32 s26, s24, 0xc000
	s_addc_u32 s27, s25, 0
	global_load_dwordx4 v[4:7], v3, s[12:13] nt
	global_load_dwordx4 v[8:11], v3, s[14:15] nt
	global_load_dwordx4 v[12:15], v3, s[16:17] nt
	global_load_dwordx4 v[16:19], v3, s[18:19] nt
	global_load_dwordx4 v[20:23], v3, s[20:21] nt
	global_load_dwordx4 v[24:27], v3, s[22:23] nt
	global_load_dwordx4 v[28:31], v3, s[24:25] nt
	global_load_dwordx4 v[32:35], v3, s[26:27] nt
	v_lshlrev_b32_e32 v36, 9, v2
	v_lshl_or_b32 v36, v1, 5, v36
	v_lshlrev_b32_e32 v37, 3, v0
	v_lshl_or_b32 v38, s2, 6, v0
	v_lshlrev_b32_e32 v38, 3, v38
	s_waitcnt vmcnt(7)
	v_lshrrev_b32_e32 v40, 16, v4
	v_and_b32_e32 v41, 0xffff, v4
	v_lshrrev_b32_e32 v42, 16, v5
	v_and_b32_e32 v43, 0xffff, v5
	v_lshrrev_b32_e32 v44, 16, v6
	v_and_b32_e32 v45, 0xffff, v6
	v_lshrrev_b32_e32 v46, 16, v7
	v_and_b32_e32 v47, 0xffff, v7
	s_waitcnt vmcnt(5)
	v_lshrrev_b32_e32 v48, 16, v8
	v_lshrrev_b32_e32 v49, 16, v12
	v_and_b32_e32 v50, 0xffff, v8
	v_and_b32_e32 v51, 0xffff, v12
	v_add3_u32 v40, v40, v48, v49
	v_add3_u32 v41, v41, v50, v51
	v_lshrrev_b32_e32 v48, 16, v9
	v_lshrrev_b32_e32 v49, 16, v13
	v_and_b32_e32 v50, 0xffff, v9
	v_and_b32_e32 v51, 0xffff, v13
	v_add3_u32 v42, v42, v48, v49
	v_add3_u32 v43, v43, v50, v51
	v_lshrrev_b32_e32 v48, 16, v10
	v_lshrrev_b32_e32 v49, 16, v14
	v_and_b32_e32 v50, 0xffff, v10
	v_and_b32_e32 v51, 0xffff, v14
	v_add3_u32 v44, v44, v48, v49
	v_add3_u32 v45, v45, v50, v51
	v_lshrrev_b32_e32 v48, 16, v11
	v_lshrrev_b32_e32 v49, 16, v15
	v_and_b32_e32 v50, 0xffff, v11
	v_and_b32_e32 v51, 0xffff, v15
	v_add3_u32 v46, v46, v48, v49
	v_add3_u32 v47, v47, v50, v51
	s_waitcnt vmcnt(3)
	v_lshrrev_b32_e32 v48, 16, v16
	v_lshrrev_b32_e32 v49, 16, v20
	v_and_b32_e32 v50, 0xffff, v16
	v_and_b32_e32 v51, 0xffff, v20
	v_add3_u32 v40, v40, v48, v49
	v_add3_u32 v41, v41, v50, v51
	v_lshrrev_b32_e32 v48, 16, v17
	v_lshrrev_b32_e32 v49, 16, v21
	v_and_b32_e32 v50, 0xffff, v17
	v_and_b32_e32 v51, 0xffff, v21
	v_add3_u32 v42, v42, v48, v49
	v_add3_u32 v43, v43, v50, v51
	v_lshrrev_b32_e32 v48, 16, v18
	v_lshrrev_b32_e32 v49, 16, v22
	v_and_b32_e32 v50, 0xffff, v18
	v_and_b32_e32 v51, 0xffff, v22
	v_add3_u32 v44, v44, v48, v49
	v_add3_u32 v45, v45, v50, v51
	v_lshrrev_b32_e32 v48, 16, v19
	v_lshrrev_b32_e32 v49, 16, v23
	v_and_b32_e32 v50, 0xffff, v19
	v_and_b32_e32 v51, 0xffff, v23
	v_add3_u32 v46, v46, v48, v49
	v_add3_u32 v47, v47, v50, v51
	s_waitcnt vmcnt(1)
	v_lshrrev_b32_e32 v48, 16, v24
	v_lshrrev_b32_e32 v49, 16, v28
	v_and_b32_e32 v50, 0xffff, v24
	v_and_b32_e32 v51, 0xffff, v28
	v_add3_u32 v40, v40, v48, v49
	v_add3_u32 v41, v41, v50, v51
	v_lshrrev_b32_e32 v48, 16, v25
	v_lshrrev_b32_e32 v49, 16, v29
	v_and_b32_e32 v50, 0xffff, v25
	v_and_b32_e32 v51, 0xffff, v29
	v_add3_u32 v42, v42, v48, v49
	v_add3_u32 v43, v43, v50, v51
	v_lshrrev_b32_e32 v48, 16, v26
	v_lshrrev_b32_e32 v49, 16, v30
	v_and_b32_e32 v50, 0xffff, v26
	v_and_b32_e32 v51, 0xffff, v30
	v_add3_u32 v44, v44, v48, v49
	v_add3_u32 v45, v45, v50, v51
	v_lshrrev_b32_e32 v48, 16, v27
	v_lshrrev_b32_e32 v49, 16, v31
	v_and_b32_e32 v50, 0xffff, v27
	v_and_b32_e32 v51, 0xffff, v31
	v_add3_u32 v46, v46, v48, v49
	v_add3_u32 v47, v47, v50, v51
	s_waitcnt vmcnt(0)
	v_lshrrev_b32_e32 v48, 16, v32
	v_and_b32_e32 v50, 0xffff, v32
	v_add_u32_e32 v40, v40, v48
	v_add_u32_e32 v41, v41, v50
	v_lshrrev_b32_e32 v48, 16, v33
	v_and_b32_e32 v50, 0xffff, v33
	v_add_u32_e32 v42, v42, v48
	v_add_u32_e32 v43, v43, v50
	v_lshrrev_b32_e32 v48, 16, v34
	v_and_b32_e32 v50, 0xffff, v34
	v_add_u32_e32 v44, v44, v48
	v_add_u32_e32 v45, v45, v50
	v_lshrrev_b32_e32 v48, 16, v35
	v_and_b32_e32 v50, 0xffff, v35
	v_add_u32_e32 v46, v46, v48
	v_add_u32_e32 v47, v47, v50
	ds_write_b128 v36, v[40:43]
	ds_write_b128 v36, v[44:47] offset:16
	v_cmp_gt_u32_e32 vcc, 64, v0
	s_waitcnt lgkmcnt(0)
	s_barrier
	s_and_saveexec_b64 s[0:1], vcc
	s_cbranch_execz .Lk4_end
	ds_read2st64_b64 v[4:7], v37 offset0:0 offset1:1
	ds_read2st64_b64 v[8:11], v37 offset0:2 offset1:3
	ds_read2st64_b64 v[12:15], v37 offset0:4 offset1:5
	ds_read2st64_b64 v[16:19], v37 offset0:6 offset1:7
	ds_read2st64_b64 v[20:23], v37 offset0:8 offset1:9
	ds_read2st64_b64 v[24:27], v37 offset0:10 offset1:11
	ds_read2st64_b64 v[28:31], v37 offset0:12 offset1:13
	ds_read2st64_b64 v[32:35], v37 offset0:14 offset1:15
	s_waitcnt lgkmcnt(6)
	v_add_u32_e32 v40, v4, v6
	v_add_u32_e32 v41, v5, v7
	v_add3_u32 v40, v40, v8, v10
	v_add3_u32 v41, v41, v9, v11
	s_waitcnt lgkmcnt(5)
	v_add3_u32 v40, v40, v12, v14
	v_add3_u32 v41, v41, v13, v15
	s_waitcnt lgkmcnt(4)
	v_add3_u32 v40, v40, v16, v18
	v_add3_u32 v41, v41, v17, v19
	s_waitcnt lgkmcnt(3)
	v_add3_u32 v40, v40, v20, v22
	v_add3_u32 v41, v41, v21, v23
	s_waitcnt lgkmcnt(2)
	v_add3_u32 v40, v40, v24, v26
	v_add3_u32 v41, v41, v25, v27
	s_waitcnt lgkmcnt(1)
	v_add3_u32 v40, v40, v28, v30
	v_add3_u32 v41, v41, v29, v31
	s_waitcnt lgkmcnt(0)
	v_add3_u32 v40, v40, v32, v34
	v_add3_u32 v41, v41, v33, v35
	global_store_dwordx2 v38, v[40:41], s[6:7]

	.amdhsa_kernel _Z9k4_reducePKjP15HIP_vector_typeIjLj2EE
		.amdhsa_group_segment_fixed_size 8192
		.amdhsa_private_segment_fixed_size 0
		.amdhsa_kernarg_size 16
		.amdhsa_user_sgpr_count 2
		.amdhsa_user_sgpr_dispatch_ptr 0
		.amdhsa_user_sgpr_queue_ptr 0
		.amdhsa_user_sgpr_kernarg_segment_ptr 1
		.amdhsa_user_sgpr_dispatch_id 0
		.amdhsa_user_sgpr_kernarg_preload_length 0
		.amdhsa_user_sgpr_kernarg_preload_offset 0
		.amdhsa_user_sgpr_private_segment_size 0
		.amdhsa_uses_dynamic_stack 0
		.amdhsa_enable_private_segment 0
		.amdhsa_system_sgpr_workgroup_id_x 1
		.amdhsa_system_sgpr_workgroup_id_y 0
		.amdhsa_system_sgpr_workgroup_id_z 0
		.amdhsa_system_sgpr_workgroup_info 0
		.amdhsa_system_vgpr_workitem_id 0
		.amdhsa_next_free_vgpr 52
		.amdhsa_next_free_sgpr 28
		.amdhsa_accum_offset 52
		.amdhsa_reserve_vcc 1
		.amdhsa_float_round_mode_32 0
		.amdhsa_float_round_mode_16_64 0
		.amdhsa_float_denorm_mode_32 3
		.amdhsa_float_denorm_mode_16_64 3
		.amdhsa_dx10_clamp 1
		.amdhsa_ieee_mode 1
		.amdhsa_fp16_overflow 0
		.amdhsa_tg_split 0
		.amdhsa_exception_fp_ieee_invalid_op 0
		.amdhsa_exception_fp_denorm_src 0
		.amdhsa_exception_fp_ieee_div_zero 0
		.amdhsa_exception_fp_ieee_overflow 0
		.amdhsa_exception_fp_ieee_underflow 0
		.amdhsa_exception_fp_ieee_inexact 0
		.amdhsa_exception_int_div_zero 0
	.end_amdhsa_kernel

.LBB4_6:
	s_waitcnt vmcnt(0)
	v_add_u32_e32 v12, v5, v3
	v_add3_u32 v28, v12, v7, v9
	v_add_u32_e32 v11, v4, v2
	v_add3_u32 v29, v11, v6, v8
	v_mbcnt_lo_u32_b32 v12, -1, 0
	v_mbcnt_hi_u32_b32 v26, -1, v12
	v_and_b32_e32 v10, 63, v0
	v_lshrrev_b32_e32 v27, 6, v0
	v_cmp_eq_u32_e64 s[2:3], 0, v10
	v_mov_b32_e32 v30, v28
	v_mov_b32_e32 v31, v29
	s_nop 0
	v_add_u32_dpp v30, v30, v30 row_shl:1 row_mask:0xf bank_mask:0xf bound_ctrl:1
	v_add_u32_dpp v31, v31, v31 row_shl:1 row_mask:0xf bank_mask:0xf bound_ctrl:1
	s_nop 0
	v_add_u32_dpp v30, v30, v30 row_shl:2 row_mask:0xf bank_mask:0xf bound_ctrl:1
	v_add_u32_dpp v31, v31, v31 row_shl:2 row_mask:0xf bank_mask:0xf bound_ctrl:1
	s_nop 0
	v_add_u32_dpp v30, v30, v30 row_shl:4 row_mask:0xf bank_mask:0xf bound_ctrl:1
	v_add_u32_dpp v31, v31, v31 row_shl:4 row_mask:0xf bank_mask:0xf bound_ctrl:1
	s_nop 0
	v_add_u32_dpp v30, v30, v30 row_shl:8 row_mask:0xf bank_mask:0xf bound_ctrl:1
	v_add_u32_dpp v31, v31, v31 row_shl:8 row_mask:0xf bank_mask:0xf bound_ctrl:1
	s_nop 0
	v_readlane_b32 s12, v30, 16
	v_readlane_b32 s13, v30, 32
	v_readlane_b32 s14, v30, 48
	v_readlane_b32 s15, v31, 16
	v_readlane_b32 s16, v31, 32
	v_readlane_b32 s17, v31, 48
	s_add_u32 s13, s13, s14
	s_add_u32 s12, s12, s13
	s_add_u32 s16, s16, s17
	s_add_u32 s15, s15, s16
	v_mov_b32_e32 v12, s14
	v_mov_b32_e32 v13, s13
	v_mov_b32_e32 v14, s12
	v_mov_b32_e32 v15, s17
	v_mov_b32_e32 v16, s16
	v_mov_b32_e32 v17, s15
	s_nop 0
	v_add_u32_dpp v30, v12, v30 quad_perm:[0,1,2,3] row_mask:0x4 bank_mask:0xf
	v_add_u32_dpp v31, v15, v31 quad_perm:[0,1,2,3] row_mask:0x4 bank_mask:0xf
	v_add_u32_dpp v30, v13, v30 quad_perm:[0,1,2,3] row_mask:0x2 bank_mask:0xf
	v_add_u32_dpp v31, v16, v31 quad_perm:[0,1,2,3] row_mask:0x2 bank_mask:0xf
	v_add_u32_dpp v30, v14, v30 quad_perm:[0,1,2,3] row_mask:0x1 bank_mask:0xf
	v_add_u32_dpp v31, v17, v31 quad_perm:[0,1,2,3] row_mask:0x1 bank_mask:0xf
	s_and_saveexec_b64 s[4:5], s[2:3]
	v_lshlrev_b32_e32 v10, 2, v27
	v_add_u32_e32 v10, 0x3000, v10
	ds_write2_b32 v10, v30, v31 offset0:32 offset1:48
	s_or_b64 exec, exec, s[4:5]
	v_mov_b32_e32 v10, 0
	s_waitcnt lgkmcnt(0)
	s_barrier
	v_sub_u32_e32 v29, v31, v29
	v_sub_u32_e32 v28, v30, v28
	v_and_b32_e32 v32, 15, v26
	v_lshlrev_b32_e32 v33, 2, v32
	ds_read_b32 v30, v33 offset:12480
	ds_read_b32 v31, v33 offset:12416
	v_cmp_gt_u32_e32 vcc, v32, v27
	s_waitcnt lgkmcnt(0)
	s_nop 0
	v_cndmask_b32_e32 v34, 0, v30, vcc
	v_cndmask_b32_e32 v35, 0, v31, vcc
	s_nop 0
	v_add_u32_dpp v30, v30, v30 row_ror:8 row_mask:0xf bank_mask:0xf bound_ctrl:1
	v_add_u32_dpp v34, v34, v34 row_ror:8 row_mask:0xf bank_mask:0xf bound_ctrl:1
	v_add_u32_dpp v35, v35, v35 row_ror:8 row_mask:0xf bank_mask:0xf bound_ctrl:1
	v_add_u32_dpp v30, v30, v30 row_ror:4 row_mask:0xf bank_mask:0xf bound_ctrl:1
	v_add_u32_dpp v34, v34, v34 row_ror:4 row_mask:0xf bank_mask:0xf bound_ctrl:1
	v_add_u32_dpp v35, v35, v35 row_ror:4 row_mask:0xf bank_mask:0xf bound_ctrl:1
	v_add_u32_dpp v30, v30, v30 row_ror:2 row_mask:0xf bank_mask:0xf bound_ctrl:1
	v_add_u32_dpp v34, v34, v34 row_ror:2 row_mask:0xf bank_mask:0xf bound_ctrl:1
	v_add_u32_dpp v35, v35, v35 row_ror:2 row_mask:0xf bank_mask:0xf bound_ctrl:1
	v_add_u32_dpp v30, v30, v30 row_ror:1 row_mask:0xf bank_mask:0xf bound_ctrl:1
	v_add_u32_dpp v34, v34, v34 row_ror:1 row_mask:0xf bank_mask:0xf bound_ctrl:1
	v_add_u32_dpp v35, v35, v35 row_ror:1 row_mask:0xf bank_mask:0xf bound_ctrl:1
	v_add_u32_e32 v29, v29, v34
	v_add_u32_e32 v28, v28, v35
	v_mov_b32_e32 v10, v30
	v_add_u32_e32 v11, v28, v9
	v_cvt_f32_u32_e32 v9, v11
	v_cvt_f32_u32_e32 v10, v10
	v_add_u32_e32 v12, v29, v8
	v_mov_b32_e32 v8, 0
	v_add_f32_e32 v13, v10, v9
	v_cmp_lt_f32_e32 vcc, 0, v13
	v_mov_b32_e32 v9, 0
	s_and_saveexec_b64 s[4:5], vcc
	s_cbranch_execz .LBB4_14
	v_add_u32_e32 v9, v12, v11
	v_cvt_f32_u32_e32 v9, v9
	v_div_scale_f32 v14, s[12:13], v13, v13, v9
	v_rcp_f32_e32 v15, v14
	v_div_scale_f32 v16, vcc, v9, v13, v9
	v_fma_f32 v17, -v14, v15, 1.0
	v_fmac_f32_e32 v15, v17, v15
	v_mul_f32_e32 v17, v16, v15
	v_fma_f32 v18, -v14, v17, v16
	v_fmac_f32_e32 v17, v18, v15
	v_fma_f32 v14, -v14, v17, v16
	v_div_fmas_f32 v14, v14, v15, v17
	v_div_fixup_f32 v9, v14, v13, v9

.LBB4_24:
	s_nop 1
	v_mov_b32_dpp v4, v2 row_ror:8 row_mask:0xf bank_mask:0xf bound_ctrl:1
	v_mov_b32_dpp v5, v3 row_ror:8 row_mask:0xf bank_mask:0xf bound_ctrl:1
	v_add_f64 v[2:3], v[2:3], v[4:5]
	s_nop 1
	v_mov_b32_dpp v4, v2 row_ror:4 row_mask:0xf bank_mask:0xf bound_ctrl:1
	v_mov_b32_dpp v5, v3 row_ror:4 row_mask:0xf bank_mask:0xf bound_ctrl:1
	v_add_f64 v[2:3], v[2:3], v[4:5]
	s_nop 1
	v_mov_b32_dpp v4, v2 row_ror:2 row_mask:0xf bank_mask:0xf bound_ctrl:1
	v_mov_b32_dpp v5, v3 row_ror:2 row_mask:0xf bank_mask:0xf bound_ctrl:1
	v_add_f64 v[2:3], v[2:3], v[4:5]
	s_nop 1
	v_mov_b32_dpp v4, v2 row_ror:1 row_mask:0xf bank_mask:0xf bound_ctrl:1
	v_mov_b32_dpp v5, v3 row_ror:1 row_mask:0xf bank_mask:0xf bound_ctrl:1
	v_add_f64 v[2:3], v[2:3], v[4:5]
	s_nop 0
	v_readlane_b32 s12, v2, 16
	v_readlane_b32 s13, v3, 16
	v_readlane_b32 s14, v2, 32
	v_readlane_b32 s15, v3, 32
	v_readlane_b32 s16, v2, 48
	v_readlane_b32 s17, v3, 48
	v_lshlrev_b32_e32 v4, 3, v27
	v_add_f64 v[0:1], v[2:3], s[12:13]
	v_add_f64 v[0:1], v[0:1], s[14:15]
	v_add_f64 v[0:1], v[0:1], s[16:17]
	s_and_saveexec_b64 s[6:7], s[2:3]
	ds_write_b64 v4, v[0:1] offset:12288

	.amdhsa_kernel _Z8k5_finalPK15HIP_vector_typeIjLj2EEPKfS4_PyPf
		.amdhsa_group_segment_fixed_size 12544
		.amdhsa_private_segment_fixed_size 0
		.amdhsa_kernarg_size 296
		.amdhsa_user_sgpr_count 2
		.amdhsa_user_sgpr_dispatch_ptr 0
		.amdhsa_user_sgpr_queue_ptr 0
		.amdhsa_user_sgpr_kernarg_segment_ptr 1
		.amdhsa_user_sgpr_dispatch_id 0
		.amdhsa_user_sgpr_kernarg_preload_length 0
		.amdhsa_user_sgpr_kernarg_preload_offset 0
		.amdhsa_user_sgpr_private_segment_size 0
		.amdhsa_uses_dynamic_stack 0
		.amdhsa_enable_private_segment 0
		.amdhsa_system_sgpr_workgroup_id_x 1
		.amdhsa_system_sgpr_workgroup_id_y 0
		.amdhsa_system_sgpr_workgroup_id_z 0
		.amdhsa_system_sgpr_workgroup_info 0
		.amdhsa_system_vgpr_workitem_id 0
		.amdhsa_next_free_vgpr 40
		.amdhsa_next_free_sgpr 24
		.amdhsa_accum_offset 40
		.amdhsa_reserve_vcc 1
		.amdhsa_float_round_mode_32 0
		.amdhsa_float_round_mode_16_64 0
		.amdhsa_float_denorm_mode_32 3
		.amdhsa_float_denorm_mode_16_64 3
		.amdhsa_dx10_clamp 1
		.amdhsa_ieee_mode 1
		.amdhsa_fp16_overflow 0
		.amdhsa_tg_split 0
		.amdhsa_exception_fp_ieee_invalid_op 0
		.amdhsa_exception_fp_denorm_src 0
		.amdhsa_exception_fp_ieee_div_zero 0
		.amdhsa_exception_fp_ieee_overflow 0
		.amdhsa_exception_fp_ieee_underflow 0
		.amdhsa_exception_fp_ieee_inexact 0
		.amdhsa_exception_int_div_zero 0
	.end_amdhsa_kernel

amdhsa.kernels:
  - .agpr_count:     0
    .args:
      - .actual_access:  read_only
        .address_space:  global
        .offset:         0
        .size:           8
        .value_kind:     global_buffer
      - .actual_access:  read_only
        .address_space:  global
        .offset:         8
        .size:           8
        .value_kind:     global_buffer
      - .address_space:  global
        .offset:         16
        .size:           8
        .value_kind:     global_buffer
      - .actual_access:  write_only
        .address_space:  global
        .offset:         24
        .size:           8
        .value_kind:     global_buffer
      - .actual_access:  write_only
        .address_space:  global
        .offset:         32
        .size:           8
        .value_kind:     global_buffer
      - .address_space:  global
        .offset:         40
        .size:           8
        .value_kind:     global_buffer
    .group_segment_fixed_size: 1648
    .kernarg_segment_align: 8
    .kernarg_segment_size: 48
    .language:       OpenCL C
    .language_version:
      - 2
      - 0
    .max_flat_workgroup_size: 768
    .name:           _Z7kf_mainPKfPKiPfPjS3_S4_
    .private_segment_fixed_size: 0
    .sgpr_count:     31
    .sgpr_spill_count: 0
    .symbol:         _Z7kf_mainPKfPKiPfPjS3_S4_.kd
    .uniform_work_group_size: 1
    .uses_dynamic_stack: false
    .vgpr_count:     160
    .vgpr_spill_count: 0
    .wavefront_size: 64
  - .agpr_count:     0
    .args:
      - .actual_access:  read_only
        .address_space:  global
        .offset:         0
        .size:           8
        .value_kind:     global_buffer
      - .actual_access:  read_only
        .address_space:  global
        .offset:         8
        .size:           8
        .value_kind:     global_buffer
      - .actual_access:  write_only
        .address_space:  global
        .offset:         16
        .size:           8
        .value_kind:     global_buffer
    .group_segment_fixed_size: 192
    .kernarg_segment_align: 8
    .kernarg_segment_size: 24
    .language:       OpenCL C
    .language_version:
      - 2
      - 0
    .max_flat_workgroup_size: 256
    .name:           _Z8k1_statsPKfPKiPf
    .private_segment_fixed_size: 0
    .sgpr_count:     48
    .sgpr_spill_count: 0
    .symbol:         _Z8k1_statsPKfPKiPf.kd
    .uniform_work_group_size: 1
    .uses_dynamic_stack: false
    .vgpr_count:     61
    .vgpr_spill_count: 0
    .wavefront_size: 64
  - .agpr_count:     0
    .args:
      - .actual_access:  read_only
        .address_space:  global
        .offset:         0
        .size:           8
        .value_kind:     global_buffer
      - .actual_access:  read_only
        .address_space:  global
        .offset:         8
        .size:           8
        .value_kind:     global_buffer
      - .actual_access:  read_only
        .address_space:  global
        .offset:         16
        .size:           8
        .value_kind:     global_buffer
      - .actual_access:  write_only
        .address_space:  global
        .offset:         24
        .size:           8
        .value_kind:     global_buffer
      - .actual_access:  write_only
        .address_space:  global
        .offset:         32
        .size:           8
        .value_kind:     global_buffer
    .group_segment_fixed_size: 1072
    .kernarg_segment_align: 8
    .kernarg_segment_size: 40
    .language:       OpenCL C
    .language_version:
      - 2
      - 0
    .max_flat_workgroup_size: 768
    .name:           _Z7k3_histPKfPKiS0_PjPf
    .private_segment_fixed_size: 0
    .sgpr_count:     51
    .sgpr_spill_count: 0
    .symbol:         _Z7k3_histPKfPKiS0_PjPf.kd
    .uniform_work_group_size: 1
    .uses_dynamic_stack: false
    .vgpr_count:     64
    .vgpr_spill_count: 0
    .wavefront_size: 64
  - .agpr_count:     0
    .args:
      - .actual_access:  read_only
        .address_space:  global
        .offset:         0
        .size:           8
        .value_kind:     global_buffer
      - .actual_access:  write_only
        .address_space:  global
        .offset:         8
        .size:           8
        .value_kind:     global_buffer
    .group_segment_fixed_size: 8192
    .kernarg_segment_align: 8
    .kernarg_segment_size: 16
    .language:       OpenCL C
    .language_version:
      - 2
      - 0
    .max_flat_workgroup_size: 256
    .name:           _Z9k4_reducePKjP15HIP_vector_typeIjLj2EE
    .private_segment_fixed_size: 0
    .sgpr_count:     34
    .sgpr_spill_count: 0
    .symbol:         _Z9k4_reducePKjP15HIP_vector_typeIjLj2EE.kd
    .uniform_work_group_size: 1
    .uses_dynamic_stack: false
    .vgpr_count:     52
    .vgpr_spill_count: 0
    .wavefront_size: 64
  - .agpr_count:     0
    .args:
      - .actual_access:  read_only
        .address_space:  global
        .offset:         0
        .size:           8
        .value_kind:     global_buffer
      - .actual_access:  read_only
        .address_space:  global
        .offset:         8
        .size:           8
        .value_kind:     global_buffer
      - .actual_access:  read_only
        .address_space:  global
        .offset:         16
        .size:           8
        .value_kind:     global_buffer
      - .address_space:  global
        .offset:         24
        .size:           8
        .value_kind:     global_buffer
      - .actual_access:  write_only
        .address_space:  global
        .offset:         32
        .size:           8
        .value_kind:     global_buffer
      - .offset:         40
        .size:           4
        .value_kind:     hidden_block_count_x
      - .offset:         44
        .size:           4
        .value_kind:     hidden_block_count_y
      - .offset:         48
        .size:           4
        .value_kind:     hidden_block_count_z
      - .offset:         52
        .size:           2
        .value_kind:     hidden_group_size_x
      - .offset:         54
        .size:           2
        .value_kind:     hidden_group_size_y
      - .offset:         56
        .size:           2
        .value_kind:     hidden_group_size_z
      - .offset:         58
        .size:           2
        .value_kind:     hidden_remainder_x
      - .offset:         60
        .size:           2
        .value_kind:     hidden_remainder_y
      - .offset:         62
        .size:           2
        .value_kind:     hidden_remainder_z
      - .offset:         80
        .size:           8
        .value_kind:     hidden_global_offset_x
      - .offset:         88
        .size:           8
        .value_kind:     hidden_global_offset_y
      - .offset:         96
        .size:           8
        .value_kind:     hidden_global_offset_z
      - .offset:         104
        .size:           2
        .value_kind:     hidden_grid_dims
    .group_segment_fixed_size: 12544
    .kernarg_segment_align: 8
    .kernarg_segment_size: 296
    .language:       OpenCL C
    .language_version:
      - 2
      - 0
    .max_flat_workgroup_size: 1024
    .name:           _Z8k5_finalPK15HIP_vector_typeIjLj2EEPKfS4_PyPf
    .private_segment_fixed_size: 0
    .sgpr_count:     30
    .sgpr_spill_count: 0
    .symbol:         _Z8k5_finalPK15HIP_vector_typeIjLj2EEPKfS4_PyPf.kd
    .uniform_work_group_size: 1
    .uses_dynamic_stack: false
    .vgpr_count:     40
    .vgpr_spill_count: 0
    .wavefront_size: 64
